# speedup vs baseline: 1.0030x; 1.0030x over previous
_Z8k_expertPKDF16_S0_PKfPcPiS0_S2_S2_S2_S2_PfS5_S4_S2_S2_S2_S2_S5_S2_S2_S2_:
	s_lshl_b32 s3, s2, 2
	s_load_dwordx8 s[8:15], s[0:1], 0x88
	s_load_dwordx2 s[70:71], s[0:1], 0x0
	s_and_b32 s3, s3, 28
	s_ashr_i32 s4, s2, 6
	s_add_i32 s34, s3, s4
	s_ashr_i32 s6, s34, 1
	v_mov_b32_e32 v2, v0
	s_lshl_b32 s4, s6, 4
	s_ashr_i32 s5, s4, 31
	v_ashrrev_i32_e32 v3, 31, v2
	s_waitcnt lgkmcnt(0)
	s_load_dwordx8 s[16:23], s[14:15], 0x0
	v_lshl_add_u64 v[4:5], v[2:3], 2, s[10:11]
	s_lshl_b64 s[10:11], s[4:5], 11
	v_lshl_add_u64 v[6:7], v[4:5], 0, s[10:11]
	s_or_b32 s10, s4, 1
	s_ashr_i32 s11, s10, 31
	s_lshl_b64 s[10:11], s[10:11], 11
	v_lshl_add_u64 v[8:9], v[4:5], 0, s[10:11]
	s_or_b32 s10, s4, 2
	s_ashr_i32 s11, s10, 31
	s_lshl_b64 s[10:11], s[10:11], 11
	v_lshl_add_u64 v[10:11], v[4:5], 0, s[10:11]
	s_or_b32 s10, s4, 3
	s_ashr_i32 s11, s10, 31
	s_lshl_b64 s[10:11], s[10:11], 11
	v_lshl_add_u64 v[12:13], v[4:5], 0, s[10:11]
	s_or_b32 s10, s4, 4
	s_ashr_i32 s11, s10, 31
	s_lshl_b64 s[10:11], s[10:11], 11
	v_lshl_add_u64 v[14:15], v[4:5], 0, s[10:11]
	s_or_b32 s10, s4, 5
	s_ashr_i32 s11, s10, 31
	s_lshl_b64 s[10:11], s[10:11], 11
	v_lshl_add_u64 v[16:17], v[4:5], 0, s[10:11]
	s_or_b32 s10, s4, 6
	s_ashr_i32 s11, s10, 31
	s_lshl_b64 s[10:11], s[10:11], 11
	v_lshl_add_u64 v[18:19], v[4:5], 0, s[10:11]
	s_or_b32 s10, s4, 7
	s_ashr_i32 s11, s10, 31
	s_lshl_b64 s[10:11], s[10:11], 11
	v_lshl_add_u64 v[20:21], v[4:5], 0, s[10:11]
	s_or_b32 s10, s4, 8
	s_ashr_i32 s11, s10, 31
	s_lshl_b64 s[10:11], s[10:11], 11
	global_load_dword v1, v[6:7], off
	global_load_dword v3, v[8:9], off
	global_load_dword v22, v[10:11], off
	global_load_dword v23, v[12:13], off
	global_load_dword v24, v[14:15], off
	global_load_dword v25, v[16:17], off
	global_load_dword v26, v[18:19], off
	global_load_dword v27, v[20:21], off
	v_lshl_add_u64 v[6:7], v[4:5], 0, s[10:11]
	s_or_b32 s10, s4, 9
	s_ashr_i32 s11, s10, 31
	s_lshl_b64 s[10:11], s[10:11], 11
	v_lshl_add_u64 v[8:9], v[4:5], 0, s[10:11]
	s_or_b32 s10, s4, 10
	s_ashr_i32 s11, s10, 31
	s_lshl_b64 s[10:11], s[10:11], 11
	v_lshl_add_u64 v[10:11], v[4:5], 0, s[10:11]
	s_or_b32 s10, s4, 11
	s_ashr_i32 s11, s10, 31
	s_lshl_b64 s[10:11], s[10:11], 11
	v_lshl_add_u64 v[12:13], v[4:5], 0, s[10:11]
	s_or_b32 s10, s4, 12
	s_ashr_i32 s11, s10, 31
	s_lshl_b64 s[10:11], s[10:11], 11
	v_lshl_add_u64 v[14:15], v[4:5], 0, s[10:11]
	s_or_b32 s10, s4, 13
	s_ashr_i32 s11, s10, 31
	s_lshl_b64 s[10:11], s[10:11], 11
	v_lshl_add_u64 v[16:17], v[4:5], 0, s[10:11]
	s_or_b32 s10, s4, 14
	s_or_b32 s4, s4, 15
	s_ashr_i32 s11, s10, 31
	s_ashr_i32 s5, s4, 31
	s_lshl_b64 s[10:11], s[10:11], 11
	s_lshl_b64 s[4:5], s[4:5], 11
	v_lshl_add_u64 v[18:19], v[4:5], 0, s[10:11]
	v_lshl_add_u64 v[4:5], v[4:5], 0, s[4:5]
	global_load_dword v20, v[6:7], off
	global_load_dword v21, v[8:9], off
	global_load_dword v28, v[10:11], off
	global_load_dword v29, v[12:13], off
	global_load_dword v30, v[14:15], off
	global_load_dword v31, v[16:17], off
	global_load_dword v32, v[18:19], off
	global_load_dword v33, v[4:5], off
	v_lshlrev_b32_e32 v4, 3, v2
	v_ashrrev_i32_e32 v5, 31, v4
	v_lshl_add_u64 v[12:13], v[4:5], 2, s[12:13]
	global_load_dwordx4 v[4:7], v[12:13], off
	global_load_dwordx4 v[8:11], v[12:13], off offset:16
	v_and_b32_e32 v200, 63, v0
	v_lshrrev_b32_e32 v201, 6, v0
	v_lshlrev_b32_e32 v202, 4, v200
	v_and_b32_e32 v203, 32, v200
	v_xor_b32_e32 v202, v202, v203
	v_lshrrev_b32_e32 v203, 6, v202
	v_lshrrev_b32_e32 v204, 1, v201
	v_lshl_add_u32 v203, v204, 4, v203
	v_and_b32_e32 v204, 62, v202
	v_and_b32_e32 v205, 1, v201
	v_lshl_add_u32 v204, v205, 6, v204
	v_lshl_add_u32 v200, v203, 12, v204
	v_add_u32_e32 v201, 0x40000, v200
	s_lshl_b32 s72, s6, 22
	s_lshr_b32 s73, s2, 4
	s_and_b32 s73, s73, 3
	s_lshl_b32 s73, s73, 20
	s_add_u32 s72, s72, s73
	s_add_u32 s74, s70, s72
	s_addc_u32 s75, s71, 0
	s_add_u32 s76, s74, 0x80000
	s_addc_u32 s77, s75, 0
	v_readfirstlane_b32 s78, v0
	s_lshl_b32 s78, s78, 4
	s_mov_b32 m0, s78
	s_add_i32 s79, s78, 0x2000
	global_load_lds_dwordx4 v200, s[74:75]
	s_mov_b32 m0, s79
	s_add_i32 s79, s78, 0x4000
	global_load_lds_dwordx4 v201, s[74:75]
	s_mov_b32 m0, s79
	s_add_i32 s79, s78, 0x6000
	global_load_lds_dwordx4 v200, s[76:77]
	s_mov_b32 m0, s79
	s_nop 0
	global_load_lds_dwordx4 v201, s[76:77]
	s_waitcnt vmcnt(21)
	v_add_f32_e32 v1, 0, v1
	s_waitcnt vmcnt(20)
	v_add_f32_e32 v1, v1, v3
	s_waitcnt vmcnt(19)
	v_add_f32_e32 v1, v1, v22
	s_waitcnt vmcnt(18)
	v_add_f32_e32 v1, v1, v23
	s_waitcnt vmcnt(17)
	v_add_f32_e32 v1, v1, v24
	s_waitcnt vmcnt(16)
	v_add_f32_e32 v1, v1, v25
	s_waitcnt vmcnt(15)
	v_add_f32_e32 v1, v1, v26
	s_waitcnt vmcnt(14)
	v_add_f32_e32 v1, v1, v27
	s_waitcnt vmcnt(13)
	v_add_f32_e32 v1, v1, v20
	s_waitcnt vmcnt(12)
	v_add_f32_e32 v1, v1, v21
	s_waitcnt vmcnt(11)
	v_add_f32_e32 v1, v1, v28
	s_waitcnt vmcnt(10)
	v_add_f32_e32 v1, v1, v29
	s_waitcnt vmcnt(9)
	v_add_f32_e32 v1, v1, v30
	s_waitcnt vmcnt(8)
	v_add_f32_e32 v1, v1, v31
	s_waitcnt vmcnt(7)
	v_add_f32_e32 v1, v1, v32
	s_waitcnt vmcnt(6)
	v_add_f32_e32 v1, v1, v33
	v_mul_f32_e32 v12, 0x3a800000, v1
	v_mbcnt_lo_u32_b32 v1, -1, 0
	v_mbcnt_hi_u32_b32 v3, -1, v1
	v_xor_b32_e32 v13, 32, v3
	v_lshlrev_b32_e32 v183, 2, v13
	v_xor_b32_e32 v13, 16, v3
	v_lshlrev_b32_e32 v181, 2, v13
	v_xor_b32_e32 v13, 8, v3
	v_lshlrev_b32_e32 v1, 2, v13
	v_xor_b32_e32 v13, 4, v3
	v_lshlrev_b32_e32 v180, 2, v13
	v_xor_b32_e32 v13, 2, v3
	v_lshlrev_b32_e32 v182, 2, v13
	v_xor_b32_e32 v13, 1, v3
	v_lshlrev_b32_e32 v184, 2, v13
	v_cmp_eq_u32_e32 vcc, 0, v3
	v_mov_b32_e32 v13, v12
	s_waitcnt vmcnt(4)
	v_pk_mul_f32 v[14:15], v[12:13], v[4:5]
	v_pk_mul_f32 v[16:17], v[12:13], v[6:7]
	v_pk_mul_f32 v[18:19], v[12:13], v[8:9]
	v_pk_mul_f32 v[20:21], v[12:13], v[10:11]
	v_add_f32_dpp v14, v14, v14 quad_perm:[1,0,3,2] row_mask:0xf bank_mask:0xf
	v_add_f32_dpp v15, v15, v15 quad_perm:[1,0,3,2] row_mask:0xf bank_mask:0xf
	v_add_f32_dpp v16, v16, v16 quad_perm:[1,0,3,2] row_mask:0xf bank_mask:0xf
	v_add_f32_dpp v17, v17, v17 quad_perm:[1,0,3,2] row_mask:0xf bank_mask:0xf
	v_add_f32_dpp v18, v18, v18 quad_perm:[1,0,3,2] row_mask:0xf bank_mask:0xf
	v_add_f32_dpp v19, v19, v19 quad_perm:[1,0,3,2] row_mask:0xf bank_mask:0xf
	v_add_f32_dpp v20, v20, v20 quad_perm:[1,0,3,2] row_mask:0xf bank_mask:0xf
	v_add_f32_dpp v21, v21, v21 quad_perm:[1,0,3,2] row_mask:0xf bank_mask:0xf
	v_add_f32_dpp v14, v14, v14 quad_perm:[2,3,0,1] row_mask:0xf bank_mask:0xf
	v_add_f32_dpp v15, v15, v15 quad_perm:[2,3,0,1] row_mask:0xf bank_mask:0xf
	v_add_f32_dpp v16, v16, v16 quad_perm:[2,3,0,1] row_mask:0xf bank_mask:0xf
	v_add_f32_dpp v17, v17, v17 quad_perm:[2,3,0,1] row_mask:0xf bank_mask:0xf
	v_add_f32_dpp v18, v18, v18 quad_perm:[2,3,0,1] row_mask:0xf bank_mask:0xf
	v_add_f32_dpp v19, v19, v19 quad_perm:[2,3,0,1] row_mask:0xf bank_mask:0xf
	v_add_f32_dpp v20, v20, v20 quad_perm:[2,3,0,1] row_mask:0xf bank_mask:0xf
	v_add_f32_dpp v21, v21, v21 quad_perm:[2,3,0,1] row_mask:0xf bank_mask:0xf
	v_add_f32_dpp v14, v14, v14 row_half_mirror row_mask:0xf bank_mask:0xf
	v_add_f32_dpp v15, v15, v15 row_half_mirror row_mask:0xf bank_mask:0xf
	v_add_f32_dpp v16, v16, v16 row_half_mirror row_mask:0xf bank_mask:0xf
	v_add_f32_dpp v17, v17, v17 row_half_mirror row_mask:0xf bank_mask:0xf
	v_add_f32_dpp v18, v18, v18 row_half_mirror row_mask:0xf bank_mask:0xf
	v_add_f32_dpp v19, v19, v19 row_half_mirror row_mask:0xf bank_mask:0xf
	v_add_f32_dpp v20, v20, v20 row_half_mirror row_mask:0xf bank_mask:0xf
	v_add_f32_dpp v21, v21, v21 row_half_mirror row_mask:0xf bank_mask:0xf
	v_add_f32_dpp v14, v14, v14 row_mirror row_mask:0xf bank_mask:0xf
	v_add_f32_dpp v15, v15, v15 row_mirror row_mask:0xf bank_mask:0xf
	v_add_f32_dpp v16, v16, v16 row_mirror row_mask:0xf bank_mask:0xf
	v_add_f32_dpp v17, v17, v17 row_mirror row_mask:0xf bank_mask:0xf
	v_add_f32_dpp v18, v18, v18 row_mirror row_mask:0xf bank_mask:0xf
	v_add_f32_dpp v19, v19, v19 row_mirror row_mask:0xf bank_mask:0xf
	v_add_f32_dpp v20, v20, v20 row_mirror row_mask:0xf bank_mask:0xf
	v_add_f32_dpp v21, v21, v21 row_mirror row_mask:0xf bank_mask:0xf
	ds_bpermute_b32 v22, v181, v14
	ds_bpermute_b32 v23, v181, v15
	ds_bpermute_b32 v24, v181, v16
	ds_bpermute_b32 v25, v181, v17
	ds_bpermute_b32 v26, v181, v18
	ds_bpermute_b32 v27, v181, v19
	ds_bpermute_b32 v28, v181, v20
	ds_bpermute_b32 v29, v181, v21
	s_waitcnt lgkmcnt(0)
	v_pk_add_f32 v[14:15], v[14:15], v[22:23]
	v_pk_add_f32 v[16:17], v[16:17], v[24:25]
	v_pk_add_f32 v[18:19], v[18:19], v[26:27]
	v_pk_add_f32 v[20:21], v[20:21], v[28:29]
	ds_bpermute_b32 v22, v183, v14
	ds_bpermute_b32 v23, v183, v15
	ds_bpermute_b32 v24, v183, v16
	ds_bpermute_b32 v25, v183, v17
	ds_bpermute_b32 v26, v183, v18
	ds_bpermute_b32 v27, v183, v19
	ds_bpermute_b32 v28, v183, v20
	ds_bpermute_b32 v29, v183, v21
	s_waitcnt lgkmcnt(0)
	v_pk_add_f32 v[14:15], v[14:15], v[22:23]
	v_pk_add_f32 v[16:17], v[16:17], v[24:25]
	v_pk_add_f32 v[18:19], v[18:19], v[26:27]
	v_pk_add_f32 v[20:21], v[20:21], v[28:29]
	s_and_saveexec_b64 s[4:5], vcc
	s_cbranch_execz .LBB5_2
	v_lshrrev_b32_e32 v22, 1, v0
	v_add_u32_e32 v22, 0x20000, v22
	ds_write_b128 v22, v[14:17]
	ds_write_b128 v22, v[18:21] offset:16
.LBB5_2:
	s_or_b64 exec, exec, s[4:5]
	s_add_i32 s3, 0, 0x20000
	v_mov_b32_e32 v2, s3
	s_add_i32 s3, 0, 0x20020
	v_mov_b32_e32 v6, s3
	s_add_i32 s3, 0, 0x20040
	s_waitcnt lgkmcnt(0)
	s_barrier
	ds_read_b128 v[2:5], v2
	ds_read_b128 v[6:9], v6
	v_mov_b32_e32 v10, s3
	s_add_i32 s3, 0, 0x20060
	v_mov_b32_e32 v14, s3
	ds_read_b128 v[10:13], v10
	ds_read_b128 v[14:17], v14
	s_waitcnt lgkmcnt(3)
	v_add_f32_e32 v2, 0, v2
	s_add_i32 s3, 0, 0x20080
	s_waitcnt lgkmcnt(2)
	v_add_f32_e32 v2, v2, v6
	v_mov_b32_e32 v6, s3
	s_add_i32 s3, 0, 0x200a0
	s_waitcnt lgkmcnt(1)
	v_add_f32_e32 v2, v2, v10
	v_mov_b32_e32 v10, s3
	ds_read_b128 v[18:21], v6
	ds_read_b128 v[22:25], v10
	s_add_i32 s3, 0, 0x200c0
	v_mov_b32_e32 v6, s3
	s_add_i32 s3, 0, 0x200e0
	v_mov_b32_e32 v10, s3
	ds_read_b128 v[26:29], v6
	ds_read_b128 v[30:33], v10
	s_waitcnt lgkmcnt(4)
	v_add_f32_e32 v2, v2, v14
	s_waitcnt lgkmcnt(0)
	v_add_f32_e32 v2, v2, v18
	v_add_f32_e32 v2, v2, v22
	v_add_f32_e32 v2, v2, v26
	v_add_f32_e32 v2, v2, v30
	v_add_f32_e32 v34, s16, v2
	v_add_f32_e32 v2, 0, v3
	v_add_f32_e32 v2, v2, v7
	v_add_f32_e32 v2, v2, v11
	v_add_f32_e32 v2, v2, v15
	v_add_f32_e32 v2, v2, v19
	v_add_f32_e32 v2, v2, v23
	v_add_f32_e32 v2, v2, v27
	v_add_f32_e32 v2, v2, v31
	v_add_f32_e32 v35, s17, v2
	v_add_f32_e32 v2, 0, v4
	v_add_f32_e32 v2, v2, v8
	v_add_f32_e32 v2, v2, v12
	v_add_f32_e32 v2, v2, v16
	v_add_f32_e32 v2, v2, v20
	v_add_f32_e32 v2, v2, v24
	v_add_f32_e32 v2, v2, v28
	v_add_f32_e32 v2, v2, v32
	v_add_f32_e32 v36, s18, v2
	v_add_f32_e32 v2, 0, v5
	v_add_f32_e32 v2, v2, v9
	v_add_f32_e32 v2, v2, v13
	v_add_f32_e32 v2, v2, v17
	v_add_f32_e32 v2, v2, v21
	v_add_f32_e32 v2, v2, v25
	s_mov_b32 s3, 0xff61b1e6
	v_add_f32_e32 v2, v2, v29
	v_max3_f32 v6, v34, s3, v35
	v_add_f32_e32 v2, v2, v33
	s_add_i32 s3, 0, 0x20010
	v_add_f32_e32 v37, s19, v2
	v_mov_b32_e32 v2, s3
	s_add_i32 s3, 0, 0x20030
	ds_read_b128 v[2:5], v2
	v_max3_f32 v38, v6, v36, v37
	v_mov_b32_e32 v6, s3
	ds_read_b128 v[6:9], v6
	s_add_i32 s3, 0, 0x20050
	v_mov_b32_e32 v10, s3
	ds_read_b128 v[10:13], v10
	s_waitcnt lgkmcnt(2)
	v_add_f32_e32 v2, 0, v2
	s_add_i32 s3, 0, 0x20070
	s_waitcnt lgkmcnt(1)
	v_add_f32_e32 v2, v2, v6
	v_mov_b32_e32 v6, s3
	ds_read_b128 v[14:17], v6
	s_add_i32 s3, 0, 0x20090
	v_mov_b32_e32 v6, s3
	s_add_i32 s3, 0, 0x200b0
	s_waitcnt lgkmcnt(1)
	v_add_f32_e32 v2, v2, v10
	v_mov_b32_e32 v10, s3
	ds_read_b128 v[18:21], v6
	ds_read_b128 v[22:25], v10
	s_add_i32 s3, 0, 0x200d0
	v_mov_b32_e32 v6, s3
	s_add_i32 s3, 0, 0x200f0
	v_mov_b32_e32 v10, s3
	ds_read_b128 v[26:29], v6
	ds_read_b128 v[30:33], v10
	s_waitcnt lgkmcnt(4)
	v_add_f32_e32 v2, v2, v14
	s_waitcnt lgkmcnt(3)
	v_add_f32_e32 v2, v2, v18
	s_waitcnt lgkmcnt(2)
	v_add_f32_e32 v2, v2, v22
	s_waitcnt lgkmcnt(1)
	v_add_f32_e32 v2, v2, v26
	s_waitcnt lgkmcnt(0)
	v_add_f32_e32 v2, v2, v30
	v_add_f32_e32 v6, s20, v2
	v_add_f32_e32 v2, 0, v3
	v_add_f32_e32 v3, 0, v4
	v_add_f32_e32 v3, v3, v8
	v_add_f32_e32 v3, v3, v12
	v_add_f32_e32 v3, v3, v16
	v_add_f32_e32 v3, v3, v20
	v_add_f32_e32 v3, v3, v24
	v_add_f32_e32 v3, v3, v28
	v_add_f32_e32 v3, v3, v32
	v_add_f32_e32 v2, v2, v7
	v_add_f32_e32 v8, s22, v3
	v_add_f32_e32 v3, 0, v5
	v_add_f32_e32 v2, v2, v11
	v_add_f32_e32 v3, v3, v9
	v_add_f32_e32 v2, v2, v15
	v_add_f32_e32 v3, v3, v13
	v_add_f32_e32 v2, v2, v19
	v_add_f32_e32 v3, v3, v17
	v_add_f32_e32 v2, v2, v23
	v_add_f32_e32 v3, v3, v21
	v_add_f32_e32 v2, v2, v27
	v_add_f32_e32 v3, v3, v25
	v_add_f32_e32 v2, v2, v31
	v_add_f32_e32 v3, v3, v29
	v_add_f32_e32 v7, s21, v2
	v_add_f32_e32 v3, v3, v33
	v_max3_f32 v2, v38, v6, v7
	v_add_f32_e32 v9, s23, v3
	v_max3_f32 v10, v2, v8, v9
	v_sub_f32_e32 v2, v34, v10
	s_mov_b32 s3, 0x3fb8aa3b
	v_mul_f32_e32 v3, 0x3fb8aa3b, v2
	v_fma_f32 v4, v2, s3, -v3
	v_rndne_f32_e32 v5, v3
	v_fmac_f32_e32 v4, 0x32a5705f, v2
	v_sub_f32_e32 v3, v3, v5
	v_add_f32_e32 v3, v3, v4
	v_exp_f32_e32 v3, v3
	v_cvt_i32_f32_e32 v4, v5
	s_mov_b32 s4, 0xc2ce8ed0
	v_cmp_ngt_f32_e32 vcc, s4, v2
	s_mov_b32 s5, 0x42b17218
	v_ldexp_f32 v3, v3, v4
	v_sub_f32_e32 v4, v35, v10
	v_mul_f32_e32 v5, 0x3fb8aa3b, v4
	v_fma_f32 v11, v4, s3, -v5
	v_rndne_f32_e32 v12, v5
	v_fmac_f32_e32 v11, 0x32a5705f, v4
	v_sub_f32_e32 v5, v5, v12
	v_add_f32_e32 v5, v5, v11
	v_exp_f32_e32 v5, v5
	v_cvt_i32_f32_e32 v11, v12
	v_cndmask_b32_e32 v3, 0, v3, vcc
	v_mov_b32_e32 v12, 0x7f800000
	v_cmp_nlt_f32_e32 vcc, s5, v2
	v_sub_f32_e32 v6, v6, v10
	v_sub_f32_e32 v7, v7, v10
	v_cndmask_b32_e32 v2, v12, v3, vcc
	v_ldexp_f32 v3, v5, v11
	v_sub_f32_e32 v5, v36, v10
	v_mul_f32_e32 v11, 0x3fb8aa3b, v5
	v_fma_f32 v13, v5, s3, -v11
	v_rndne_f32_e32 v14, v11
	v_fmac_f32_e32 v13, 0x32a5705f, v5
	v_sub_f32_e32 v11, v11, v14
	v_add_f32_e32 v11, v11, v13
	v_exp_f32_e32 v11, v11
	v_cvt_i32_f32_e32 v13, v14
	v_cmp_ngt_f32_e32 vcc, s4, v4
	v_sub_f32_e32 v8, v8, v10
	v_sub_f32_e32 v9, v9, v10
	v_cndmask_b32_e32 v3, 0, v3, vcc
	v_cmp_nlt_f32_e32 vcc, s5, v4
	v_ldexp_f32 v4, v11, v13
	v_sub_f32_e32 v11, v37, v10
	v_mul_f32_e32 v13, 0x3fb8aa3b, v11
	v_fma_f32 v15, v11, s3, -v13
	v_rndne_f32_e32 v16, v13
	v_fmac_f32_e32 v15, 0x32a5705f, v11
	v_sub_f32_e32 v13, v13, v16
	v_add_f32_e32 v13, v13, v15
	v_exp_f32_e32 v13, v13
	v_cvt_i32_f32_e32 v15, v16
	v_cndmask_b32_e32 v3, v12, v3, vcc
	v_cmp_ngt_f32_e32 vcc, s4, v5
	v_add_f32_e32 v14, v2, v3
	v_mul_f32_e32 v10, 0x3fb8aa3b, v9
	v_cndmask_b32_e32 v4, 0, v4, vcc
	v_cmp_nlt_f32_e32 vcc, s5, v5
	v_ldexp_f32 v5, v13, v15
	v_mul_f32_e32 v13, 0x3fb8aa3b, v6
	v_fma_f32 v15, v6, s3, -v13
	v_rndne_f32_e32 v16, v13
	v_fmac_f32_e32 v15, 0x32a5705f, v6
	v_sub_f32_e32 v13, v13, v16
	v_add_f32_e32 v13, v13, v15
	v_cndmask_b32_e32 v4, v12, v4, vcc
	v_cmp_ngt_f32_e32 vcc, s4, v11
	v_exp_f32_e32 v13, v13
	v_cvt_i32_f32_e32 v15, v16
	v_cndmask_b32_e32 v5, 0, v5, vcc
	v_cmp_nlt_f32_e32 vcc, s5, v11
	v_add_f32_e32 v14, v4, v14
	v_ldexp_f32 v13, v13, v15
	v_cndmask_b32_e32 v5, v12, v5, vcc
	v_add_f32_e32 v11, v5, v14
	v_mul_f32_e32 v14, 0x3fb8aa3b, v7
	v_fma_f32 v15, v7, s3, -v14
	v_rndne_f32_e32 v16, v14
	v_fmac_f32_e32 v15, 0x32a5705f, v7
	v_sub_f32_e32 v14, v14, v16
	v_add_f32_e32 v14, v14, v15
	v_exp_f32_e32 v14, v14
	v_cvt_i32_f32_e32 v15, v16
	v_cmp_ngt_f32_e32 vcc, s4, v6
	s_bfe_u32 s33, s2, 0x30003
	s_load_dwordx4 s[28:31], s[0:1], 0x0
	v_cndmask_b32_e32 v13, 0, v13, vcc
	v_cmp_nlt_f32_e32 vcc, s5, v6
	s_nop 1
	v_cndmask_b32_e32 v6, v12, v13, vcc
	v_ldexp_f32 v13, v14, v15
	v_mul_f32_e32 v14, 0x3fb8aa3b, v8
	v_fma_f32 v15, v8, s3, -v14
	v_rndne_f32_e32 v16, v14
	v_fmac_f32_e32 v15, 0x32a5705f, v8
	v_sub_f32_e32 v14, v14, v16
	v_add_f32_e32 v14, v14, v15
	v_exp_f32_e32 v14, v14
	v_cvt_i32_f32_e32 v15, v16
	v_cmp_ngt_f32_e32 vcc, s4, v7
	v_add_f32_e32 v11, v6, v11
	s_nop 0
	v_cndmask_b32_e32 v13, 0, v13, vcc
	v_cmp_nlt_f32_e32 vcc, s5, v7
	s_nop 1
	v_cndmask_b32_e32 v7, v12, v13, vcc
	v_ldexp_f32 v13, v14, v15
	v_fma_f32 v14, v9, s3, -v10
	v_rndne_f32_e32 v15, v10
	v_fmac_f32_e32 v14, 0x32a5705f, v9
	v_sub_f32_e32 v10, v10, v15
	v_add_f32_e32 v10, v10, v14
	v_exp_f32_e32 v10, v10
	v_cvt_i32_f32_e32 v14, v15
	v_cmp_ngt_f32_e32 vcc, s4, v8
	v_add_f32_e32 v11, v7, v11
	v_ldexp_f32 v10, v10, v14
	v_cndmask_b32_e32 v13, 0, v13, vcc
	v_cmp_nlt_f32_e32 vcc, s5, v8
	s_nop 1
	v_cndmask_b32_e32 v8, v12, v13, vcc
	v_cmp_ngt_f32_e32 vcc, s4, v9
	v_add_f32_e32 v11, v8, v11
	s_nop 0
	v_cndmask_b32_e32 v10, 0, v10, vcc
	v_cmp_nlt_f32_e32 vcc, s5, v9
	s_nop 1
	v_cndmask_b32_e32 v9, v12, v10, vcc
	v_add_f32_e32 v10, v9, v11
	v_div_scale_f32 v11, s[4:5], v10, v10, 1.0
	v_rcp_f32_e32 v12, v11
	s_nop 0
	v_fma_f32 v13, -v11, v12, 1.0
	v_fmac_f32_e32 v12, v13, v12
	v_div_scale_f32 v13, vcc, 1.0, v10, 1.0
	v_mul_f32_e32 v14, v13, v12
	v_fma_f32 v15, -v11, v14, v13
	v_fmac_f32_e32 v14, v15, v12
	v_fma_f32 v11, -v11, v14, v13
	v_div_fmas_f32 v11, v11, v12, v14
	v_div_fixup_f32 v10, v11, v10, 1.0
	v_pk_mul_f32 v[2:3], v[2:3], v[10:11] op_sel_hi:[1,0]
	s_nop 0
	v_cmp_nlt_f32_e32 vcc, -1.0, v2
	s_nop 1
	v_cndmask_b32_e64 v11, v2, -1.0, vcc
	v_cmp_gt_f32_e64 s[4:5], v3, v11
	s_nop 1
	v_cndmask_b32_e64 v11, v11, v3, s[4:5]
	v_pk_mul_f32 v[4:5], v[4:5], v[10:11] op_sel_hi:[1,0]
	v_cndmask_b32_e64 v12, 0, 1, s[4:5]
	v_cmp_gt_f32_e64 s[4:5], v4, v11
	v_readfirstlane_b32 s3, v12
	s_nop 0
	v_cndmask_b32_e64 v11, v11, v4, s[4:5]
	s_and_b64 s[4:5], s[4:5], exec
	v_cmp_gt_f32_e64 s[4:5], v5, v11
	s_cselect_b32 s3, 2, s3
	s_nop 0
	v_cndmask_b32_e64 v11, v11, v5, s[4:5]
	s_and_b64 s[4:5], s[4:5], exec
	v_pk_mul_f32 v[6:7], v[6:7], v[10:11] op_sel_hi:[1,0]
	s_cselect_b32 s3, 3, s3
	v_cmp_gt_f32_e64 s[4:5], v6, v11
	s_nop 1
	v_cndmask_b32_e64 v11, v11, v6, s[4:5]
	s_and_b64 s[4:5], s[4:5], exec
	v_cmp_gt_f32_e64 s[4:5], v7, v11
	s_cselect_b32 s3, 4, s3
	s_nop 0
	v_cndmask_b32_e64 v11, v11, v7, s[4:5]
	s_and_b64 s[4:5], s[4:5], exec
	v_pk_mul_f32 v[8:9], v[8:9], v[10:11] op_sel_hi:[1,0]
	s_cselect_b32 s3, 5, s3
	v_cmp_gt_f32_e64 s[4:5], v8, v11
	s_nop 1
	v_cndmask_b32_e64 v10, v11, v8, s[4:5]
	s_and_b64 s[4:5], s[4:5], exec
	v_cmp_ngt_f32_e64 s[4:5], v9, v10
	s_cselect_b32 s3, 6, s3
	s_and_b64 s[10:11], s[4:5], exec
	s_cselect_b32 s3, s3, 7
	s_cmp_eq_u32 s3, 0
	s_cselect_b64 s[10:11], -1, 0
	s_or_b64 s[10:11], vcc, s[10:11]
	v_cndmask_b32_e64 v11, v2, -1.0, s[10:11]
	s_cmp_lg_u32 s3, 1
	s_cselect_b64 s[10:11], -1, 0
	v_cmp_gt_f32_e32 vcc, v3, v11
	s_and_b64 vcc, s[10:11], vcc
	s_cmp_lg_u32 s3, 2
	v_cndmask_b32_e32 v11, v11, v3, vcc
	v_cndmask_b32_e64 v12, 0, 1, vcc
	s_cselect_b64 s[10:11], -1, 0
	v_cmp_gt_f32_e32 vcc, v4, v11
	s_and_b64 vcc, s[10:11], vcc
	s_and_b64 s[10:11], vcc, exec
	v_readfirstlane_b32 s7, v12
	v_cndmask_b32_e32 v11, v11, v4, vcc
	s_cselect_b32 s7, 2, s7
	s_cmp_lg_u32 s3, 3
	s_cselect_b64 s[10:11], -1, 0
	v_cmp_gt_f32_e32 vcc, v5, v11
	s_and_b64 vcc, s[10:11], vcc
	s_and_b64 s[10:11], vcc, exec
	v_cndmask_b32_e32 v11, v11, v5, vcc
	s_cselect_b32 s7, 3, s7
	s_cmp_lg_u32 s3, 4
	s_cselect_b64 s[10:11], -1, 0
	v_cmp_gt_f32_e32 vcc, v6, v11
	s_and_b64 vcc, s[10:11], vcc
	s_and_b64 s[10:11], vcc, exec
	v_cndmask_b32_e32 v11, v11, v6, vcc
	s_cselect_b32 s7, 4, s7
	s_cmp_lg_u32 s3, 5
	s_cselect_b64 s[10:11], -1, 0
	v_cmp_gt_f32_e32 vcc, v7, v11
	s_and_b64 vcc, s[10:11], vcc
	s_and_b64 s[10:11], vcc, exec
	v_cndmask_b32_e32 v11, v11, v7, vcc
	s_cselect_b32 s7, 5, s7
	s_cmp_lg_u32 s3, 6
	s_cselect_b64 s[10:11], -1, 0
	v_cmp_gt_f32_e32 vcc, v8, v11
	s_and_b64 vcc, s[10:11], vcc
	s_and_b64 s[10:11], vcc, exec
	v_cndmask_b32_e32 v11, v11, v8, vcc
	v_cmp_gt_f32_e32 vcc, v9, v11
	s_cselect_b32 s7, 6, s7
	s_and_b64 vcc, s[4:5], vcc
	v_cndmask_b32_e64 v10, v9, v10, s[4:5]
	v_cndmask_b32_e32 v11, v11, v9, vcc
	v_add_f32_e32 v12, v10, v11
	v_add_f32_e32 v12, 0x322bcc77, v12
	v_div_scale_f32 v13, s[4:5], v12, v12, v10
	v_rcp_f32_e32 v14, v13
	s_and_b64 s[4:5], vcc, exec
	s_cselect_b32 s7, 7, s7
	s_and_b32 s35, s2, 64
	v_fma_f32 v15, -v13, v14, 1.0
	v_fmac_f32_e32 v14, v15, v14
	v_div_scale_f32 v15, vcc, v10, v12, v10
	v_mul_f32_e32 v16, v15, v14
	v_fma_f32 v17, -v13, v16, v15
	v_fmac_f32_e32 v16, v17, v14
	v_fma_f32 v13, -v13, v16, v15
	v_div_scale_f32 v15, s[4:5], v12, v12, v11
	v_rcp_f32_e32 v17, v15
	v_div_fmas_f32 v13, v13, v14, v16
	v_div_fixup_f32 v10, v13, v12, v10
	v_fma_f32 v13, -v15, v17, 1.0
	v_fmac_f32_e32 v17, v13, v17
	v_div_scale_f32 v13, vcc, v11, v12, v11
	v_mul_f32_e32 v14, v13, v17
	v_fma_f32 v16, -v15, v14, v13
	v_fmac_f32_e32 v14, v16, v17
	v_fma_f32 v13, -v15, v14, v13
	v_div_fmas_f32 v13, v13, v17, v14
	v_readfirstlane_b32 s12, v10
	v_or_b32_e32 v10, s35, v0
	v_div_fixup_f32 v11, v13, v12, v11
	v_or_b32_e32 v10, s33, v10
	v_readfirstlane_b32 s13, v11
	v_cmp_eq_u32_e32 vcc, 0, v10
	s_and_saveexec_b64 s[4:5], vcc
	s_cbranch_execz .LBB5_4
	s_lshl_b32 s10, s6, 3
	s_ashr_i32 s11, s10, 31
	s_lshl_b64 s[10:11], s[10:11], 2
	s_add_u32 s10, s8, s10
	s_addc_u32 s11, s9, s11
	v_mov_b32_e32 v10, 0x1000
	global_store_dwordx4 v10, v[2:5], s[10:11] offset:512
	global_store_dwordx4 v10, v[6:9], s[10:11] offset:528
